# 1664 (was 832) layer-1 expert-weight tiles converted in the in-projection slot
# baseline (speedup 1.0000x reference)
; #define LAS __attribute__((address_space(3)))
; DI void phase_p0(const Args& A, LAS unsigned char* lds, int it0, int it1, int gw, int ngw, int wave, int lane) {
;     ...
;     auto desc = [&](int item) { F8Tile d; const int r = item - I_IN - I_OUT; const int le = r / (3 * I_E), q = r % (3 * I_E), which = q / I_E, t = q % I_E;
;         if (which < 2) { const int kb = t / 44, nb = t % 44, n0 = nb * 64;
;             d.W = A.in[which == 0 ? I_EW1 : I_EW3] + (size_t)le * DM * FF; d.N = FF; d.k0 = kb * 128; d.n0 = n0; d.dst = w13 + (size_t)le * 5632 * DM; d.Kd = DM; d.drow0 = (size_t)((n0 >> 7) * 256 + which * 128 + (n0 & 127)); }
;         else { const int kb = t / 16, nb = t % 16;
;             d.W = A.in[I_EW2] + (size_t)le * FF * DM; d.N = DM; d.k0 = kb * 128; d.n0 = nb * 64; d.dst = w2t + (size_t)le * DM * FF; d.Kd = FF; d.drow0 = (size_t)nb * 64; }
;         return d; };
;     if (it < it1) {
;         f32x4 ra[4][4], rb[4][4]; LAS unsigned char* sc8 = (LAS unsigned char*)scr;
;         F8Tile d = desc(it);
; template <int l> DI void run_layer(const Args& A, LAS unsigned char* lds, const XcdBarrier& bar, int lo, int hi, int G, int bid, int tid, int lane, int wave, int gw, int ngw, int gtid, int nthr) {
;     ...
;         const bool conv = (l == 0) && (G >= 2 * P0_XC1) && (G % 8 == 0); const int Gg = conv ? G - P0_XC1 : G;
;         if (conv && bid >= Gg) { __syncthreads(); phase_p0(A, lds, P0_W, P0_SPLIT, (bid - Gg) * NWAVES + wave, P0_XC1 * NWAVES, wave, lane); __syncthreads(); }
.LBB0_135:
	v_readlane_b32 s4, v235, 9
	v_readlane_b32 s6, v235, 11
	s_cmp_lt_i32 s6, 3
	v_readlane_b32 s7, v235, 12
	s_cselect_b64 s[0:1], -1, 0
	s_cmp_gt_i32 s6, 2
	v_readlane_b32 s5, v235, 10
	s_cselect_b64 s[2:3], -1, 0
	s_cmp_lt_i32 s7, 3
	s_cselect_b64 s[4:5], -1, 0
	s_or_b64 s[2:3], s[2:3], s[4:5]
	s_and_b64 vcc, exec, s[2:3]
	s_cbranch_vccnz .LBB0_194
	s_cmpk_lt_i32 s50, 0xd0
	v_readlane_b32 s4, v235, 57
	s_cselect_b64 s[2:3], -1, 0
	s_cmp_lg_u32 s4, 0
	s_cselect_b64 s[4:5], -1, 0
	s_or_b64 s[2:3], s[2:3], s[4:5]
	s_add_i32 s6, s50, 0xffffff93
	s_and_b64 s[4:5], s[2:3], exec
	s_cselect_b32 s28, s50, s6
	s_cmp_lt_i32 s92, s28
	s_cselect_b64 s[4:5], -1, 0
	s_or_b64 s[4:5], s[2:3], s[4:5]
	s_mov_b64 s[2:3], -1
	s_and_b64 vcc, exec, s[4:5]
	s_cbranch_vccnz .LBB0_169
	s_sub_i32 s2, s92, s28
	s_lshl_b32 s2, s2, 3
	v_readlane_b32 s3, v235, 52
	s_add_i32 s2, s2, s3
	s_cmpk_gt_u32 s2, 0x487f
	s_barrier
	s_cbranch_scc1 .LBB0_168
	v_readlane_b32 s4, v235, 9
	v_readlane_b32 s5, v235, 10
	s_add_u32 s20, s4, 0x1600000
	s_addc_u32 s21, s5, 0
	s_add_u32 s22, s4, 0x17600000
	s_addc_u32 s23, s5, 0
	s_and_b32 s3, s2, 0xffff
	s_mul_i32 s3, s3, 0xf83f
	s_lshr_b32 s5, s3, 26
	s_mul_i32 s3, s5, 0x420
	v_readlane_b32 s7, v235, 12
	s_sub_i32 s2, s2, s3
	s_and_b32 s7, s2, 0xffff
	s_mul_i32 s3, s7, 0xba2f
	s_lshr_b32 s3, s3, 24
	s_mulk_i32 s3, 0x160
	s_sub_i32 s12, s2, s3
	s_cmpk_gt_u32 s7, 0x2bf
	v_readlane_b32 s6, v235, 11
	s_cbranch_scc0 .LBB0_141
	s_and_b32 s3, 0xffff, s5
	v_readlane_b32 s36, v235, 0
	s_and_b32 s2, 0xffff, s12
	s_mul_i32 s4, s3, 0xb00000
	v_readlane_b32 s38, v235, 2
	v_readlane_b32 s39, v235, 3
	s_add_u32 s8, s38, s4
	s_addc_u32 s9, s39, 0
	s_lshl_b32 s4, s2, 3
	s_lshl_b32 s2, s2, 6
	s_and_b32 s6, s4, 0xf80
	s_and_b32 s4, s2, 0x3c0
	s_mul_i32 s3, s3, 0x2c0000
	s_add_u32 s10, s22, s3
	v_readlane_b32 s37, v235, 1
	v_readlane_b32 s40, v235, 4
	v_readlane_b32 s41, v235, 5
	v_readlane_b32 s42, v235, 6
	v_readlane_b32 s43, v235, 7
	s_addc_u32 s11, s23, 0
	s_cbranch_execz .LBB0_142
	v_mov_b32_e32 v130, s4
	s_movk_i32 s24, 0xb00
	s_movk_i32 s18, 0x400
	s_branch .LBB0_143

; DI void phase_p0(const Args& A, LAS unsigned char* lds, int it0, int it1, int gw, int ngw, int wave, int lane) {
;     ...
;     auto desc = [&](int item) { F8Tile d; const int r = item - I_IN - I_OUT; const int le = r / (3 * I_E), q = r % (3 * I_E), which = q / I_E, t = q % I_E;
;         if (which < 2) { const int kb = t / 44, nb = t % 44, n0 = nb * 64;
;             d.W = A.in[which == 0 ? I_EW1 : I_EW3] + (size_t)le * DM * FF; d.N = FF; d.k0 = kb * 128; d.n0 = n0; d.dst = w13 + (size_t)le * 5632 * DM; d.Kd = DM; d.drow0 = (size_t)((n0 >> 7) * 256 + which * 128 + (n0 & 127)); }
;         else { const int kb = t / 16, nb = t % 16;
;             d.W = A.in[I_EW2] + (size_t)le * FF * DM; d.N = DM; d.k0 = kb * 128; d.n0 = nb * 64; d.dst = w2t + (size_t)le * DM * FF; d.Kd = FF; d.drow0 = (size_t)nb * 64; }
;     ...
;         for (; it < it1; it += ngw) {
;             const bool vn = it + ngw < it1; F8Tile dn = d; if (vn) dn = desc(it + ngw);
.LBB0_145:
	s_add_i32 s26, s2, 0x368
	s_cmpk_lt_i32 s26, 0x4f40
	s_cselect_b64 s[16:17], -1, 0
	s_cmpk_gt_i32 s26, 0x4f3f
	s_cselect_b64 s[14:15], -1, 0
	s_and_b64 vcc, exec, s[14:15]
	s_mov_b32 s27, s6
	s_cbranch_vccnz .LBB0_152
	s_addk_i32 s2, 0xfca8
	s_mul_hi_i32 s3, s2, 0x3e0f83e1
	s_lshr_b32 s4, s3, 31
	s_ashr_i32 s7, s3, 8
	s_add_i32 s7, s7, s4
	s_mul_i32 s3, s7, 0x420
	s_sub_i32 s29, s2, s3
	s_mul_i32 s2, s29, 0xba3
	s_lshr_b32 s3, s2, 31
	s_ashr_i32 s34, s2, 20
	s_add_i32 s34, s34, s3
	s_mul_i32 s2, s34, 0x160
	s_sub_i32 s33, s29, s2
	s_mov_b64 s[18:19], -1
	s_cmpk_gt_i32 s29, 0x2bf
	s_sext_i32_i16 s35, s33
	s_mul_hi_i32 s30, s7, 0xb00000
	s_mul_i32 s31, s7, 0xb00000
	s_cbranch_scc0 .LBB0_148
	v_readlane_b32 s36, v235, 0
	v_readlane_b32 s38, v235, 2
	v_readlane_b32 s39, v235, 3
	s_add_u32 s8, s38, s31
	s_addc_u32 s9, s39, s30
	s_lshl_b32 s2, s35, 3
	s_and_b32 s27, s2, 0xf80
	s_lshl_b32 s2, s35, 6
	s_and_b32 s4, s2, 0x3c0
	s_mul_i32 s3, s7, 0x2c0000
	s_mul_hi_i32 s2, s7, 0x2c0000
	s_add_u32 s12, s22, s3
	v_readlane_b32 s37, v235, 1
	v_readlane_b32 s40, v235, 4
	v_readlane_b32 s41, v235, 5
	v_readlane_b32 s42, v235, 6
	v_readlane_b32 s43, v235, 7
	s_addc_u32 s13, s23, s2
	s_mov_b64 s[18:19], 0
	s_mov_b64 s[2:3], s[4:5]

; #define LAS __attribute__((address_space(3)))
; DI void phase_p0(const Args& A, LAS unsigned char* lds, int it0, int it1, int gw, int ngw, int wave, int lane) {
;     ...
;     if (it < it1) {
;         f32x4 ra[4][4], rb[4][4]; LAS unsigned char* sc8 = (LAS unsigned char*)scr;
;         F8Tile d = desc(it);
; template <int l> DI void run_layer(const Args& A, LAS unsigned char* lds, const XcdBarrier& bar, int lo, int hi, int G, int bid, int tid, int lane, int wave, int gw, int ngw, int gtid, int nthr) {
;     ...
;         const bool conv = (l == 0) && (P0_SPLIT < P0_END) && (G >= 2 * P0_XC) && (G % 8 == 0); const int Gg = conv ? G - P0_XC : G;
;         if (conv && bid >= Gg) { __syncthreads(); phase_p0(A, lds, P0_SPLIT, P0_END, (bid - Gg) * NWAVES + wave, P0_XC * NWAVES, wave, lane); __syncthreads(); }
.LBB0_1337:
	s_cmp_lt_i32 s6, 10
	s_cselect_b64 s[8:9], -1, 0
	s_and_b64 s[0:1], s[8:9], s[0:1]
	s_andn2_b64 vcc, exec, s[0:1]
	s_cbranch_vccnz .LBB0_1395
	s_cmpk_lt_i32 s50, 0xa0
	v_readlane_b32 s2, v235, 57
	s_cselect_b64 s[0:1], -1, 0
	s_cmp_lg_u32 s2, 0
	s_cselect_b64 s[2:3], -1, 0
	s_or_b64 s[0:1], s[0:1], s[2:3]
	s_add_i32 s4, s50, 0xffffffb0
	s_and_b64 s[2:3], s[0:1], exec
	s_cselect_b32 s30, s50, s4
	s_cmp_lt_i32 s92, s30
	s_cselect_b64 s[2:3], -1, 0
	s_or_b64 s[2:3], s[0:1], s[2:3]
	s_mov_b64 s[0:1], -1
	s_and_b64 vcc, exec, s[2:3]
	s_cbranch_vccnz .LBB0_1371
	s_sub_i32 s0, s92, s30
	s_lshl_b32 s0, s0, 3
	v_readlane_b32 s1, v235, 52
	s_add_i32 s0, s0, s1
	s_cmpk_gt_u32 s0, 0x3b7f
	s_waitcnt vmcnt(0)
	s_barrier
	s_cbranch_scc1 .LBB0_1370
	v_readlane_b32 s4, v235, 9
	v_readlane_b32 s5, v235, 10
	s_add_u32 s18, s4, 0x1600000
	s_addc_u32 s19, s5, 0
	s_add_u32 s20, s4, 0x17600000
	s_addc_u32 s21, s5, 0
	s_addk_i32 s0, 0x4880
	s_and_b32 s1, s0, 0xffff
	s_mul_i32 s1, s1, 0xf83f
	s_lshr_b32 s1, s1, 26
	s_mul_i32 s2, s1, 0x420
	s_sub_i32 s0, s0, s2
	s_and_b32 s5, s0, 0xffff
	s_mul_i32 s2, s5, 0xba2f
	s_lshr_b32 s2, s2, 24
	s_mulk_i32 s2, 0x160
	s_sub_i32 s12, s0, s2
	s_cmpk_gt_u32 s5, 0x2bf
	v_readlane_b32 s6, v235, 11
	v_readlane_b32 s7, v235, 12
	s_cbranch_scc0 .LBB0_1343
	s_and_b32 s2, 0xffff, s1
	v_readlane_b32 s36, v235, 0
	s_and_b32 s0, 0xffff, s12
	s_mul_i32 s3, s2, 0xb00000
	v_readlane_b32 s38, v235, 2
	v_readlane_b32 s39, v235, 3
	s_add_u32 s6, s38, s3
	s_addc_u32 s7, s39, 0
	s_lshl_b32 s3, s0, 3
	s_lshl_b32 s0, s0, 6
	s_and_b32 s4, s3, 0xf80
	s_and_b32 s0, s0, 0x3c0
	s_mul_i32 s2, s2, 0x2c0000
	s_add_u32 s10, s20, s2
	v_readlane_b32 s37, v235, 1
	v_readlane_b32 s40, v235, 4
	v_readlane_b32 s41, v235, 5
	v_readlane_b32 s42, v235, 6
	v_readlane_b32 s43, v235, 7
	s_addc_u32 s11, s21, 0
	s_cbranch_execz .LBB0_1344
	v_mov_b32_e32 v130, s0
	s_movk_i32 s22, 0xb00
	s_movk_i32 s16, 0x400
	s_branch .LBB0_1345

; DI void f8_load(f32x4 (&v)[4][4], const F8Tile& d, int hb, int lane) {
;     const int nq = lane & 15, kq = lane >> 4;
; #pragma unroll
;     for (int it = 0; it < 4; ++it)
; #pragma unroll
;         for (int j = 0; j < 4; ++j) v[it][j] = __builtin_nontemporal_load((const f32x4*)(d.W + (size_t)(d.k0 + hb * 64 + it * 16 + kq * 4 + j) * d.N + d.n0 + 4 * nq));
; }
.LBB0_1345:
	v_lshrrev_b32_e32 v2, 2, v146
	v_and_b32_e32 v1, 12, v2
	v_or_b32_e32 v187, 0x72, v1
	v_or_b32_e32 v188, 0x73, v2
	v_mov_b32_e32 v135, 0
	v_or_b32_e32 v159, 3, v2
	v_or_b32_e32 v163, 19, v2
	v_or_b32_e32 v167, 35, v2
	v_or_b32_e32 v172, 51, v2
	v_or_b32_e32 v176, 0x43, v2
	v_or_b32_e32 v180, 0x53, v2
	v_or_b32_e32 v184, 0x63, v2
	v_add_u32_e32 v2, s4, v188
	v_add_u32_e32 v4, s4, v187
	s_mov_b32 s1, 0
	v_lshlrev_b32_e32 v3, 2, v0
	v_mul_u32_u24_e32 v134, s16, v2
	v_mul_u32_u24_e32 v4, s16, v4
	v_mov_b32_e32 v5, v135
	v_and_b32_e32 v132, 60, v3
	v_lshl_add_u64 v[2:3], v[134:135], 2, s[6:7]
	s_lshl_b64 s[2:3], s[0:1], 2
	v_lshl_add_u64 v[4:5], v[4:5], 2, s[6:7]
	v_lshl_add_u64 v[2:3], v[2:3], 0, s[2:3]
	v_lshlrev_b32_e32 v134, 2, v132
	v_lshl_add_u64 v[4:5], v[4:5], 0, s[2:3]
	v_or_b32_e32 v183, 0x62, v1
	v_or_b32_e32 v185, 0x70, v1
	v_or_b32_e32 v186, 0x71, v1
	v_lshl_add_u64 v[2:3], v[2:3], 0, v[134:135]
	v_lshl_add_u64 v[4:5], v[4:5], 0, v[134:135]
	global_load_dwordx4 v[10:13], v[2:3], off nt
	global_load_dwordx4 v[14:17], v[4:5], off nt
	v_add_u32_e32 v2, s4, v186
	v_add_u32_e32 v4, s4, v185
	v_add_u32_e32 v18, s4, v184
	v_add_u32_e32 v20, s4, v183
	v_mul_u32_u24_e32 v2, s16, v2
	v_mov_b32_e32 v3, v135
	v_mul_u32_u24_e32 v4, s16, v4
	v_mov_b32_e32 v5, v135
	v_mul_u32_u24_e32 v18, s16, v18
	v_mov_b32_e32 v19, v135
	v_mul_u32_u24_e32 v20, s16, v20
	v_mov_b32_e32 v21, v135
	v_lshl_add_u64 v[2:3], v[2:3], 2, s[6:7]
	v_lshl_add_u64 v[4:5], v[4:5], 2, s[6:7]
	v_lshl_add_u64 v[18:19], v[18:19], 2, s[6:7]
	v_lshl_add_u64 v[20:21], v[20:21], 2, s[6:7]
	v_lshl_add_u64 v[2:3], v[2:3], 0, s[2:3]
	v_lshl_add_u64 v[4:5], v[4:5], 0, s[2:3]
	v_lshl_add_u64 v[18:19], v[18:19], 0, s[2:3]
	v_lshl_add_u64 v[20:21], v[20:21], 0, s[2:3]
	v_or_b32_e32 v179, 0x52, v1
	v_or_b32_e32 v181, 0x60, v1
	v_or_b32_e32 v182, 0x61, v1
	v_lshl_add_u64 v[2:3], v[2:3], 0, v[134:135]
	v_lshl_add_u64 v[6:7], v[4:5], 0, v[134:135]
	v_lshl_add_u64 v[18:19], v[18:19], 0, v[134:135]
	v_lshl_add_u64 v[20:21], v[20:21], 0, v[134:135]
	global_load_dwordx4 v[2:5], v[2:3], off nt
	s_nop 0
	global_load_dwordx4 v[6:9], v[6:7], off nt
	s_nop 0
	global_load_dwordx4 v[26:29], v[18:19], off nt
	global_load_dwordx4 v[30:33], v[20:21], off nt
	v_add_u32_e32 v18, s4, v182
	v_add_u32_e32 v20, s4, v181
	v_add_u32_e32 v34, s4, v180
	v_add_u32_e32 v36, s4, v179
	v_mul_u32_u24_e32 v18, s16, v18
	v_mov_b32_e32 v19, v135
	v_mul_u32_u24_e32 v20, s16, v20
	v_mov_b32_e32 v21, v135
	v_mul_u32_u24_e32 v34, s16, v34
	v_mov_b32_e32 v35, v135
	v_mul_u32_u24_e32 v36, s16, v36
	v_mov_b32_e32 v37, v135
	v_lshl_add_u64 v[18:19], v[18:19], 2, s[6:7]
	v_lshl_add_u64 v[20:21], v[20:21], 2, s[6:7]
	v_lshl_add_u64 v[34:35], v[34:35], 2, s[6:7]
	v_lshl_add_u64 v[36:37], v[36:37], 2, s[6:7]
	v_lshl_add_u64 v[18:19], v[18:19], 0, s[2:3]
	v_lshl_add_u64 v[20:21], v[20:21], 0, s[2:3]
	v_lshl_add_u64 v[34:35], v[34:35], 0, s[2:3]
	v_lshl_add_u64 v[36:37], v[36:37], 0, s[2:3]
	v_or_b32_e32 v175, 0x42, v1
	v_or_b32_e32 v177, 0x50, v1
	v_or_b32_e32 v178, 0x51, v1
	v_lshl_add_u64 v[18:19], v[18:19], 0, v[134:135]
	v_lshl_add_u64 v[22:23], v[20:21], 0, v[134:135]
	v_lshl_add_u64 v[34:35], v[34:35], 0, v[134:135]
	v_lshl_add_u64 v[36:37], v[36:37], 0, v[134:135]
	global_load_dwordx4 v[18:21], v[18:19], off nt
	s_nop 0
	global_load_dwordx4 v[22:25], v[22:23], off nt
	s_nop 0
	global_load_dwordx4 v[42:45], v[34:35], off nt
	global_load_dwordx4 v[46:49], v[36:37], off nt
	v_add_u32_e32 v34, s4, v178
	v_add_u32_e32 v36, s4, v177
	v_add_u32_e32 v50, s4, v176
	v_add_u32_e32 v52, s4, v175
	v_mul_u32_u24_e32 v34, s16, v34
	v_mov_b32_e32 v35, v135
	v_mul_u32_u24_e32 v36, s16, v36
	v_mov_b32_e32 v37, v135
	v_mul_u32_u24_e32 v50, s16, v50
	v_mov_b32_e32 v51, v135
	v_mul_u32_u24_e32 v52, s16, v52
	v_mov_b32_e32 v53, v135
	v_lshl_add_u64 v[34:35], v[34:35], 2, s[6:7]
	v_lshl_add_u64 v[36:37], v[36:37], 2, s[6:7]
	v_lshl_add_u64 v[50:51], v[50:51], 2, s[6:7]
	v_lshl_add_u64 v[52:53], v[52:53], 2, s[6:7]
	v_lshl_add_u64 v[34:35], v[34:35], 0, s[2:3]
	v_lshl_add_u64 v[36:37], v[36:37], 0, s[2:3]
	v_lshl_add_u64 v[50:51], v[50:51], 0, s[2:3]
	v_lshl_add_u64 v[52:53], v[52:53], 0, s[2:3]
	v_or_b32_e32 v171, 50, v1
	v_or_b32_e32 v173, 64, v1
	v_or_b32_e32 v174, 0x41, v1
	v_lshl_add_u64 v[34:35], v[34:35], 0, v[134:135]
	v_lshl_add_u64 v[38:39], v[36:37], 0, v[134:135]
	v_lshl_add_u64 v[50:51], v[50:51], 0, v[134:135]
	v_lshl_add_u64 v[52:53], v[52:53], 0, v[134:135]
	global_load_dwordx4 v[34:37], v[34:35], off nt
	s_nop 0
	global_load_dwordx4 v[38:41], v[38:39], off nt
	s_nop 0
	global_load_dwordx4 v[58:61], v[50:51], off nt
	global_load_dwordx4 v[62:65], v[52:53], off nt
	v_add_u32_e32 v50, s4, v174
	v_add_u32_e32 v52, s4, v173
	v_add_u32_e32 v66, s4, v172
	v_add_u32_e32 v68, s4, v171
	v_mul_u32_u24_e32 v50, s16, v50
	v_mov_b32_e32 v51, v135
	v_mul_u32_u24_e32 v52, s16, v52
	v_mov_b32_e32 v53, v135
	v_mul_u32_u24_e32 v66, s16, v66
	v_mov_b32_e32 v67, v135
	v_mul_u32_u24_e32 v68, s16, v68
	v_mov_b32_e32 v69, v135
	v_lshl_add_u64 v[50:51], v[50:51], 2, s[6:7]
	v_lshl_add_u64 v[52:53], v[52:53], 2, s[6:7]
	v_lshl_add_u64 v[66:67], v[66:67], 2, s[6:7]
	v_lshl_add_u64 v[68:69], v[68:69], 2, s[6:7]
	v_lshl_add_u64 v[50:51], v[50:51], 0, s[2:3]
	v_lshl_add_u64 v[52:53], v[52:53], 0, s[2:3]
	v_lshl_add_u64 v[66:67], v[66:67], 0, s[2:3]
	v_lshl_add_u64 v[68:69], v[68:69], 0, s[2:3]
	v_or_b32_e32 v166, 34, v1
	v_or_b32_e32 v168, 48, v1
	v_or_b32_e32 v169, 49, v1
	v_lshl_add_u64 v[50:51], v[50:51], 0, v[134:135]
	v_lshl_add_u64 v[54:55], v[52:53], 0, v[134:135]
	v_lshl_add_u64 v[66:67], v[66:67], 0, v[134:135]
; #define LAS __attribute__((address_space(3)))
; DI void f8_load(f32x4 (&v)[4][4], const F8Tile& d, int hb, int lane) {
;     const int nq = lane & 15, kq = lane >> 4;
; #pragma unroll
;     for (int it = 0; it < 4; ++it)
; #pragma unroll
;         for (int j = 0; j < 4; ++j) v[it][j] = __builtin_nontemporal_load((const f32x4*)(d.W + (size_t)(d.k0 + hb * 64 + it * 16 + kq * 4 + j) * d.N + d.n0 + 4 * nq));
; }
; DI void phase_p0(const Args& A, LAS unsigned char* lds, int it0, int it1, int gw, int ngw, int wave, int lane) {
;     ...
;     if (it < it1) {
;         f32x4 ra[4][4], rb[4][4]; LAS unsigned char* sc8 = (LAS unsigned char*)scr;
;         F8Tile d = desc(it);
;         f8_load(ra, d, 0, lane); f8_load(rb, d, 1, lane);
;         for (; it < it1; it += ngw) {
;             const bool vn = it + ngw < it1; F8Tile dn = d; if (vn) dn = desc(it + ngw);
;             f8_convert_reload(ra, 0, F8_WSC, sc8, vn, dn, lane);
	v_lshl_add_u64 v[68:69], v[68:69], 0, v[134:135]
	global_load_dwordx4 v[50:53], v[50:51], off nt
	s_nop 0
	global_load_dwordx4 v[54:57], v[54:55], off nt
	s_nop 0
	global_load_dwordx4 v[78:81], v[66:67], off nt
	global_load_dwordx4 v[74:77], v[68:69], off nt
	v_add_u32_e32 v66, s4, v169
	v_add_u32_e32 v68, s4, v168
	v_add_u32_e32 v82, s4, v167
	v_add_u32_e32 v84, s4, v166
	v_mul_u32_u24_e32 v66, s16, v66
	v_mov_b32_e32 v67, v135
	v_mul_u32_u24_e32 v68, s16, v68
	v_mov_b32_e32 v69, v135
	v_mul_u32_u24_e32 v82, s16, v82
	v_mov_b32_e32 v83, v135
	v_mul_u32_u24_e32 v84, s16, v84
	v_mov_b32_e32 v85, v135
	v_lshl_add_u64 v[66:67], v[66:67], 2, s[6:7]
	v_lshl_add_u64 v[68:69], v[68:69], 2, s[6:7]
	v_lshl_add_u64 v[82:83], v[82:83], 2, s[6:7]
	v_lshl_add_u64 v[84:85], v[84:85], 2, s[6:7]
	v_lshl_add_u64 v[66:67], v[66:67], 0, s[2:3]
	v_lshl_add_u64 v[68:69], v[68:69], 0, s[2:3]
	v_lshl_add_u64 v[82:83], v[82:83], 0, s[2:3]
	v_lshl_add_u64 v[84:85], v[84:85], 0, s[2:3]
	v_or_b32_e32 v162, 18, v1
	v_or_b32_e32 v164, 32, v1
	v_or_b32_e32 v165, 33, v1
	v_lshl_add_u64 v[66:67], v[66:67], 0, v[134:135]
	v_lshl_add_u64 v[70:71], v[68:69], 0, v[134:135]
	v_lshl_add_u64 v[82:83], v[82:83], 0, v[134:135]
	v_lshl_add_u64 v[84:85], v[84:85], 0, v[134:135]
	global_load_dwordx4 v[66:69], v[66:67], off nt
	s_nop 0
	global_load_dwordx4 v[70:73], v[70:71], off nt
	s_nop 0
	global_load_dwordx4 v[90:93], v[82:83], off nt
	global_load_dwordx4 v[94:97], v[84:85], off nt
	v_add_u32_e32 v82, s4, v165
	v_add_u32_e32 v84, s4, v164
	v_add_u32_e32 v98, s4, v163
	v_add_u32_e32 v100, s4, v162
	v_mul_u32_u24_e32 v82, s16, v82
	v_mov_b32_e32 v83, v135
	v_mul_u32_u24_e32 v84, s16, v84
	v_mov_b32_e32 v85, v135
	v_mul_u32_u24_e32 v98, s16, v98
	v_mov_b32_e32 v99, v135
	v_mul_u32_u24_e32 v100, s16, v100
	v_mov_b32_e32 v101, v135
	v_lshl_add_u64 v[82:83], v[82:83], 2, s[6:7]
	v_lshl_add_u64 v[84:85], v[84:85], 2, s[6:7]
	v_lshl_add_u64 v[98:99], v[98:99], 2, s[6:7]
	v_lshl_add_u64 v[100:101], v[100:101], 2, s[6:7]
	v_lshl_add_u64 v[82:83], v[82:83], 0, s[2:3]
	v_lshl_add_u64 v[84:85], v[84:85], 0, s[2:3]
	v_lshl_add_u64 v[98:99], v[98:99], 0, s[2:3]
	v_lshl_add_u64 v[100:101], v[100:101], 0, s[2:3]
	v_or_b32_e32 v158, 2, v1
	v_or_b32_e32 v160, 16, v1
	v_or_b32_e32 v161, 17, v1
	v_lshl_add_u64 v[82:83], v[82:83], 0, v[134:135]
	v_lshl_add_u64 v[86:87], v[84:85], 0, v[134:135]
	v_lshl_add_u64 v[98:99], v[98:99], 0, v[134:135]
	v_lshl_add_u64 v[100:101], v[100:101], 0, v[134:135]
	global_load_dwordx4 v[82:85], v[82:83], off nt
	s_nop 0
	global_load_dwordx4 v[86:89], v[86:87], off nt
	s_nop 0
	global_load_dwordx4 v[106:109], v[98:99], off nt
	global_load_dwordx4 v[110:113], v[100:101], off nt
	v_add_u32_e32 v98, s4, v161
	v_add_u32_e32 v100, s4, v160
	v_add_u32_e32 v114, s4, v159
	v_add_u32_e32 v116, s4, v158
	v_mul_u32_u24_e32 v98, s16, v98
	v_mov_b32_e32 v99, v135
	v_mul_u32_u24_e32 v100, s16, v100
	v_mov_b32_e32 v101, v135
	v_mul_u32_u24_e32 v114, s16, v114
	v_mov_b32_e32 v115, v135
	v_mul_u32_u24_e32 v116, s16, v116
	v_mov_b32_e32 v117, v135
	v_lshl_add_u64 v[98:99], v[98:99], 2, s[6:7]
	v_lshl_add_u64 v[100:101], v[100:101], 2, s[6:7]
	v_lshl_add_u64 v[114:115], v[114:115], 2, s[6:7]
	v_lshl_add_u64 v[116:117], v[116:117], 2, s[6:7]
	v_lshl_add_u64 v[98:99], v[98:99], 0, s[2:3]
	v_lshl_add_u64 v[100:101], v[100:101], 0, s[2:3]
	v_lshl_add_u64 v[114:115], v[114:115], 0, s[2:3]
	v_lshl_add_u64 v[116:117], v[116:117], 0, s[2:3]
	v_or_b32_e32 v133, 1, v1
	v_lshl_add_u64 v[98:99], v[98:99], 0, v[134:135]
	v_lshl_add_u64 v[102:103], v[100:101], 0, v[134:135]
	v_lshl_add_u64 v[114:115], v[114:115], 0, v[134:135]
	v_lshl_add_u64 v[116:117], v[116:117], 0, v[134:135]
	global_load_dwordx4 v[98:101], v[98:99], off nt
	s_nop 0
	global_load_dwordx4 v[102:105], v[102:103], off nt
	s_nop 0
	global_load_dwordx4 v[122:125], v[114:115], off nt
	global_load_dwordx4 v[126:129], v[116:117], off nt
	v_add_u32_e32 v114, s4, v133
	v_add_u32_e32 v116, s4, v1
	v_mul_u32_u24_e32 v114, s16, v114
	v_mov_b32_e32 v115, v135
	v_mul_u32_u24_e32 v116, s16, v116
	v_mov_b32_e32 v117, v135
	v_lshl_add_u64 v[114:115], v[114:115], 2, s[6:7]
	v_lshl_add_u64 v[116:117], v[116:117], 2, s[6:7]
	v_lshl_add_u64 v[114:115], v[114:115], 0, s[2:3]
	v_lshl_add_u64 v[116:117], v[116:117], 0, s[2:3]
	v_lshl_add_u64 v[114:115], v[114:115], 0, v[134:135]
	v_lshl_add_u64 v[118:119], v[116:117], 0, v[134:135]
	global_load_dwordx4 v[114:117], v[114:115], off nt
	s_nop 0
	global_load_dwordx4 v[118:121], v[118:119], off nt
	v_readlane_b32 s2, v235, 52
	s_mulk_i32 s2, 0x4200
	v_lshlrev_b32_e32 v137, 4, v0
	s_add_i32 s2, s2, 0
	v_and_b32_e32 v138, 0x70, v137
	v_add_u32_e32 v134, s2, v1
	v_lshrrev_b32_e32 v136, 3, v146
	v_add_u32_e32 v157, s2, v138
	s_lshl_b32 s2, s30, 3
	v_readlane_b32 s12, v235, 54
	v_mov_b32_e32 v131, v135
	v_mul_u32_u24_e32 v156, 0x84, v132
	v_mul_u32_u24_e32 v189, 0x84, v136
	v_readlane_b32 s13, v235, 55
	s_sub_i32 s2, s12, s2
	v_mov_b32_e32 v139, v135
	v_mov_b32_e32 v137, v135
	v_or_b32_e32 v140, 8, v136
	v_mov_b32_e32 v141, v135
	v_or_b32_e32 v142, 16, v136
	v_mov_b32_e32 v143, v135
	v_or_b32_e32 v144, 24, v136
	v_mov_b32_e32 v145, v135
	v_or_b32_e32 v148, 32, v136
	v_mov_b32_e32 v149, v135
	v_or_b32_e32 v150, 40, v136
	v_mov_b32_e32 v151, v135
	v_or_b32_e32 v152, 48, v136
	v_mov_b32_e32 v153, v135
	v_or_b32_e32 v154, 56, v136
	v_mov_b32_e32 v155, v135
	s_add_i32 s23, s2, 0x4b00
	s_mov_b32 s24, 0xc3e00000
	v_add_u32_e32 v189, v157, v189
	v_mov_b32_e32 v190, 0x43e00000
	v_add_u32_e32 v191, v134, v156
	v_mov_b64_e32 v[156:157], v[130:131]
	s_mov_b32 s17, s22
	s_mov_b64 s[12:13], s[10:11]
	s_waitcnt vmcnt(0)
	s_branch .LBB0_1347
